# baseline (speedup 1.0000x reference)
.Lq_noprio:
	s_waitcnt vmcnt(28)
	v_cvt_pk_f16_f32 v164, v36, v40
	v_cvt_pk_f16_f32 v180, v68, v72
	v_pk_add_f16 v164, v164, -0.5 op_sel_hi:[1,0]
	v_pk_add_f16 v180, v180, -0.5 op_sel_hi:[1,0]
	v_pk_mul_f16 v196, v180, v180
	v_pk_mul_f16 v212, v164, v180
	v_pk_fma_f16 v196, v164, v164, v196
	v_cvt_pk_f16_f32 v168, v37, v41
	v_cvt_pk_f16_f32 v184, v69, v73
	v_pk_add_f16 v168, v168, -0.5 op_sel_hi:[1,0]
	v_pk_add_f16 v184, v184, -0.5 op_sel_hi:[1,0]
	v_pk_mul_f16 v200, v184, v184
	v_pk_mul_f16 v216, v168, v184
	v_pk_fma_f16 v200, v168, v168, v200
	v_cvt_pk_f16_f32 v172, v38, v42
	v_cvt_pk_f16_f32 v188, v70, v74
	v_pk_add_f16 v172, v172, -0.5 op_sel_hi:[1,0]
	v_pk_add_f16 v188, v188, -0.5 op_sel_hi:[1,0]
	v_pk_mul_f16 v204, v188, v188
	v_pk_mul_f16 v220, v172, v188
	v_pk_fma_f16 v204, v172, v172, v204
	v_cvt_pk_f16_f32 v176, v39, v43
	v_cvt_pk_f16_f32 v192, v71, v75
	v_pk_add_f16 v176, v176, -0.5 op_sel_hi:[1,0]
	v_pk_add_f16 v192, v192, -0.5 op_sel_hi:[1,0]
	v_pk_mul_f16 v208, v192, v192
	v_pk_mul_f16 v224, v176, v192
	v_pk_fma_f16 v208, v176, v176, v208
	s_waitcnt vmcnt(24)
	v_cvt_pk_f16_f32 v165, v44, v48
	v_cvt_pk_f16_f32 v181, v76, v80
	v_pk_add_f16 v165, v165, -0.5 op_sel_hi:[1,0]
	v_pk_add_f16 v181, v181, -0.5 op_sel_hi:[1,0]
	v_pk_mul_f16 v197, v181, v181
	v_pk_mul_f16 v213, v165, v181
	v_pk_fma_f16 v197, v165, v165, v197
	v_cvt_pk_f16_f32 v169, v45, v49
	v_cvt_pk_f16_f32 v185, v77, v81
	v_pk_add_f16 v169, v169, -0.5 op_sel_hi:[1,0]
	v_pk_add_f16 v185, v185, -0.5 op_sel_hi:[1,0]
	v_pk_mul_f16 v201, v185, v185
	v_pk_mul_f16 v217, v169, v185
	v_pk_fma_f16 v201, v169, v169, v201
	v_cvt_pk_f16_f32 v173, v46, v50
	v_cvt_pk_f16_f32 v189, v78, v82
	v_pk_add_f16 v173, v173, -0.5 op_sel_hi:[1,0]
	v_pk_add_f16 v189, v189, -0.5 op_sel_hi:[1,0]
	v_pk_mul_f16 v205, v189, v189
	v_pk_mul_f16 v221, v173, v189
	v_pk_fma_f16 v205, v173, v173, v205
	v_cvt_pk_f16_f32 v177, v47, v51
	v_cvt_pk_f16_f32 v193, v79, v83
	v_pk_add_f16 v177, v177, -0.5 op_sel_hi:[1,0]
	v_pk_add_f16 v193, v193, -0.5 op_sel_hi:[1,0]
	v_pk_mul_f16 v209, v193, v193
	v_pk_mul_f16 v225, v177, v193
	v_pk_fma_f16 v209, v177, v177, v209
	s_waitcnt vmcnt(20)
	v_cvt_pk_f16_f32 v166, v52, v56
	v_cvt_pk_f16_f32 v182, v84, v88
	v_pk_add_f16 v166, v166, -0.5 op_sel_hi:[1,0]
	v_pk_add_f16 v182, v182, -0.5 op_sel_hi:[1,0]
	v_pk_mul_f16 v198, v182, v182
	v_pk_mul_f16 v214, v166, v182
	v_pk_fma_f16 v198, v166, v166, v198
	v_cvt_pk_f16_f32 v170, v53, v57
	v_cvt_pk_f16_f32 v186, v85, v89
	v_pk_add_f16 v170, v170, -0.5 op_sel_hi:[1,0]
	v_pk_add_f16 v186, v186, -0.5 op_sel_hi:[1,0]
	v_pk_mul_f16 v202, v186, v186
	v_pk_mul_f16 v218, v170, v186
	v_pk_fma_f16 v202, v170, v170, v202
	v_cvt_pk_f16_f32 v174, v54, v58
	v_cvt_pk_f16_f32 v190, v86, v90
	v_pk_add_f16 v174, v174, -0.5 op_sel_hi:[1,0]
	v_pk_add_f16 v190, v190, -0.5 op_sel_hi:[1,0]
	v_pk_mul_f16 v206, v190, v190
	v_pk_mul_f16 v222, v174, v190
	v_pk_fma_f16 v206, v174, v174, v206
	v_cvt_pk_f16_f32 v178, v55, v59
	v_cvt_pk_f16_f32 v194, v87, v91
	v_pk_add_f16 v178, v178, -0.5 op_sel_hi:[1,0]
	v_pk_add_f16 v194, v194, -0.5 op_sel_hi:[1,0]
	v_pk_mul_f16 v210, v194, v194
	v_pk_mul_f16 v226, v178, v194
	v_pk_fma_f16 v210, v178, v178, v210
	s_waitcnt vmcnt(16)
	v_cvt_pk_f16_f32 v167, v60, v64
	v_cvt_pk_f16_f32 v183, v92, v96
	v_pk_add_f16 v167, v167, -0.5 op_sel_hi:[1,0]
	v_pk_add_f16 v183, v183, -0.5 op_sel_hi:[1,0]
	v_pk_mul_f16 v199, v183, v183
	v_pk_mul_f16 v215, v167, v183
	v_pk_fma_f16 v199, v167, v167, v199
	v_cvt_pk_f16_f32 v171, v61, v65
	v_cvt_pk_f16_f32 v187, v93, v97
	v_pk_add_f16 v171, v171, -0.5 op_sel_hi:[1,0]
	v_pk_add_f16 v187, v187, -0.5 op_sel_hi:[1,0]
	v_pk_mul_f16 v203, v187, v187
	v_pk_mul_f16 v219, v171, v187
	v_pk_fma_f16 v203, v171, v171, v203
	v_cvt_pk_f16_f32 v175, v62, v66
	v_cvt_pk_f16_f32 v191, v94, v98
	v_pk_add_f16 v175, v175, -0.5 op_sel_hi:[1,0]
	v_pk_add_f16 v191, v191, -0.5 op_sel_hi:[1,0]
	v_pk_mul_f16 v207, v191, v191
	v_pk_mul_f16 v223, v175, v191
	v_pk_fma_f16 v207, v175, v175, v207
	v_cvt_pk_f16_f32 v179, v63, v67
	v_cvt_pk_f16_f32 v195, v95, v99
	v_pk_add_f16 v179, v179, -0.5 op_sel_hi:[1,0]
	v_pk_add_f16 v195, v195, -0.5 op_sel_hi:[1,0]
	v_pk_mul_f16 v211, v195, v195
	v_pk_mul_f16 v227, v179, v195
	v_pk_fma_f16 v211, v179, v179, v211
	v_mfma_f32_16x16x32_f16 v[68:71], v[164:167], v[24:27], 0
	v_mfma_f32_16x16x32_f16 v[72:75], v[168:171], v[24:27], 0
	v_mfma_f32_16x16x32_f16 v[76:79], v[172:175], v[24:27], 0
	v_mfma_f32_16x16x32_f16 v[80:83], v[176:179], v[24:27], 0
	v_mfma_f32_16x16x32_f16 v[84:87], v[180:183], v[24:27], 0
	v_mfma_f32_16x16x32_f16 v[88:91], v[184:187], v[24:27], 0
	v_mfma_f32_16x16x32_f16 v[92:95], v[188:191], v[24:27], 0
	v_mfma_f32_16x16x32_f16 v[96:99], v[192:195], v[24:27], 0
	s_nop 1
	v_cvt_pk_f16_f32 v36, v68, v72
	s_nop 0
	v_cvt_pk_f16_f32 v37, v76, v80
	v_cvt_pk_f16_f32 v38, v69, v73
	v_cvt_pk_f16_f32 v39, v77, v81
	v_cvt_pk_f16_f32 v40, v70, v74
	v_cvt_pk_f16_f32 v41, v78, v82
	v_cvt_pk_f16_f32 v42, v71, v75
	v_cvt_pk_f16_f32 v43, v79, v83
	v_mfma_f32_16x16x32_f16 v[68:71], v[196:199], v[24:27], 0
	v_mfma_f32_16x16x32_f16 v[72:75], v[200:203], v[24:27], 0
	v_mfma_f32_16x16x32_f16 v[76:79], v[204:207], v[24:27], 0
	v_mfma_f32_16x16x32_f16 v[80:83], v[208:211], v[24:27], 0
	v_cvt_pk_f16_f32 v44, v84, v88
	v_cvt_pk_f16_f32 v45, v92, v96
	v_cvt_pk_f16_f32 v46, v85, v89
	v_cvt_pk_f16_f32 v47, v93, v97
	v_cvt_pk_f16_f32 v48, v86, v90
	v_cvt_pk_f16_f32 v49, v94, v98
	v_cvt_pk_f16_f32 v50, v87, v91
	v_cvt_pk_f16_f32 v51, v95, v99
	v_mfma_f32_16x16x32_f16 v[84:87], v[212:215], v[24:27], 0
	v_mfma_f32_16x16x32_f16 v[88:91], v[216:219], v[24:27], 0
	v_mfma_f32_16x16x32_f16 v[92:95], v[220:223], v[24:27], 0
	v_mfma_f32_16x16x32_f16 v[96:99], v[224:227], v[24:27], 0
	v_cvt_pk_f16_f32 v52, v68, v72
	v_cvt_pk_f16_f32 v53, v76, v80
	v_cvt_pk_f16_f32 v54, v69, v73
	v_cvt_pk_f16_f32 v55, v77, v81
	v_cvt_pk_f16_f32 v56, v70, v74
	v_cvt_pk_f16_f32 v57, v78, v82
	v_cvt_pk_f16_f32 v58, v71, v75
	v_cvt_pk_f16_f32 v59, v79, v83
	v_cvt_pk_f16_f32 v60, v84, v88
	v_cvt_pk_f16_f32 v61, v92, v96
	v_cvt_pk_f16_f32 v62, v85, v89
	v_cvt_pk_f16_f32 v63, v93, v97
	v_cvt_pk_f16_f32 v64, v86, v90
	v_cvt_pk_f16_f32 v65, v94, v98
	v_cvt_pk_f16_f32 v66, v87, v91
	v_cvt_pk_f16_f32 v67, v95, v99
	s_mov_b64 exec, s[38:39]
	ds_write_b128 v4, v[40:43] offset:0
	ds_write_b128 v4, v[48:51] offset:512
	ds_write_b128 v4, v[56:59] offset:1024
	ds_write_b128 v4, v[64:67] offset:1536
	s_mov_b64 exec, -1
	v_mfma_f32_16x16x32_f16 v[68:71], v[24:27], v[36:39], 0
	v_mfma_f32_16x16x32_f16 v[72:75], v[24:27], v[44:47], 0
	v_mfma_f32_16x16x32_f16 v[76:79], v[24:27], v[52:55], v[0:3]
	v_mfma_f32_16x16x32_f16 v[80:83], v[24:27], v[60:63], 0
	v_mfma_f32_16x16x32_f16 v[84:87], v[28:31], v[36:39], 0
	v_mfma_f32_16x16x32_f16 v[88:91], v[28:31], v[44:47], 0
	v_mfma_f32_16x16x32_f16 v[92:95], v[28:31], v[52:55], v[0:3]
	v_mfma_f32_16x16x32_f16 v[96:99], v[28:31], v[60:63], 0
	v_mfma_f32_16x16x32_f16 v[84:87], v[32:35], v[40:43], v[84:87]
	v_mfma_f32_16x16x32_f16 v[88:91], v[32:35], v[48:51], v[88:91]
	v_mfma_f32_16x16x32_f16 v[92:95], v[32:35], v[56:59], v[92:95]
	v_mfma_f32_16x16x32_f16 v[96:99], v[32:35], v[64:67], v[96:99]
	s_waitcnt lgkmcnt(0)
	ds_write_b32 v6, v6 offset:0
	ds_read_b32 v9, v7 offset:0
	v_mul_f32_e32 v244, v68, v72
	v_mul_f32_e32 v247, v69, v73
	v_mul_f32_e32 v250, v70, v74
	v_mul_f32_e32 v253, v71, v75
	v_mul_f32_e64 v245, -v72, v72
	v_mul_f32_e64 v248, -v73, v73
	v_mul_f32_e64 v251, -v74, v74
	v_mul_f32_e64 v254, -v75, v75
	v_add_f32_e32 v246, v68, v72
	v_add_f32_e32 v249, v69, v73
	v_add_f32_e32 v252, v70, v74
	v_add_f32_e32 v255, v71, v75
	v_fma_f32 v245, -v68, v68, v245
	v_fma_f32 v248, -v69, v69, v248
	v_fma_f32 v251, -v70, v70, v251
	v_fma_f32 v254, -v71, v71, v254
	v_fma_f32 v68, v10, v246, v11
	v_fma_f32 v69, v10, v249, v11
	v_fma_f32 v70, v10, v252, v11
	v_fma_f32 v71, v10, v255, v11
	v_fma_f32 v80, v13, v80, v14
	v_fma_f32 v81, v13, v81, v14
	v_fma_f32 v82, v13, v82, v14
	v_fma_f32 v83, v13, v83, v14
	v_fma_f32 v76, v12, v76, v245
	v_fma_f32 v77, v12, v77, v248
	v_fma_f32 v78, v12, v78, v251
	v_fma_f32 v79, v12, v79, v254
	v_fma_f32 v72, 2.0, v244, v68
	v_fma_f32 v73, 2.0, v247, v69
	v_fma_f32 v74, 2.0, v250, v70
	v_fma_f32 v75, 2.0, v253, v71
	v_sub_f32_e32 v68, v68, v245
	v_sub_f32_e32 v69, v69, v248
	v_sub_f32_e32 v70, v70, v251
	v_sub_f32_e32 v71, v71, v254
	v_fma_f32 v80, -2.0, v244, v80
	v_fma_f32 v81, -2.0, v247, v81
	v_fma_f32 v82, -2.0, v250, v82
	v_fma_f32 v83, -2.0, v253, v83
	v_mul_f32_e32 v68, v68, v76
	v_mul_f32_e32 v69, v69, v77
	v_mul_f32_e32 v70, v70, v78
	v_mul_f32_e32 v71, v71, v79
	v_rcp_f32_e32 v68, v68
	v_rcp_f32_e32 v69, v69
	v_rcp_f32_e32 v70, v70
	v_rcp_f32_e32 v71, v71
	v_mul_f32_e32 v72, v72, v80
	v_mul_f32_e32 v73, v73, v81
	v_mul_f32_e32 v74, v74, v82
	v_mul_f32_e32 v75, v75, v83
	v_fma_f32 v19, v72, v68, v19
	v_fma_f32 v20, v73, v69, v20
	v_fma_f32 v21, v74, v70, v21
	v_fma_f32 v22, v75, v71, v22
	v_mfma_f32_16x16x32_f16 v[68:71], v[24:27], v[40:43], 0
	v_mfma_f32_16x16x32_f16 v[72:75], v[24:27], v[48:51], 0
	v_mfma_f32_16x16x32_f16 v[76:79], v[24:27], v[56:59], v[0:3]
	v_mfma_f32_16x16x32_f16 v[80:83], v[24:27], v[64:67], 0
	s_barrier
	ds_read_b32 v9, v7 offset:0
	s_waitcnt lgkmcnt(0)
	v_cmp_ne_u32_e32 vcc, 0, v9
	s_cbranch_vccnz .Lq_go_0

.Lq_go_0:
	ds_read_b128 v[228:231], v5 offset:0
	ds_read_b128 v[232:235], v5 offset:512
	ds_read_b128 v[236:239], v5 offset:1024
	ds_read_b128 v[240:243], v5 offset:1536
	v_mul_f32_e32 v244, v84, v88
	v_mul_f32_e32 v247, v85, v89
	v_mul_f32_e32 v250, v86, v90
	v_mul_f32_e32 v253, v87, v91
	v_mul_f32_e64 v245, -v88, v88
	v_mul_f32_e64 v248, -v89, v89
	v_mul_f32_e64 v251, -v90, v90
	v_mul_f32_e64 v254, -v91, v91
	v_add_f32_e32 v246, v84, v88
	v_add_f32_e32 v249, v85, v89
	v_add_f32_e32 v252, v86, v90
	v_add_f32_e32 v255, v87, v91
	v_fma_f32 v245, -v84, v84, v245
	v_fma_f32 v248, -v85, v85, v248
	v_fma_f32 v251, -v86, v86, v251
	v_fma_f32 v254, -v87, v87, v254
	v_fma_f32 v84, v10, v246, v11
	v_fma_f32 v85, v10, v249, v11
	v_fma_f32 v86, v10, v252, v11
	v_fma_f32 v87, v10, v255, v11
	v_fma_f32 v96, v13, v96, v14
	v_fma_f32 v97, v13, v97, v14
	v_fma_f32 v98, v13, v98, v14
	v_fma_f32 v99, v13, v99, v14
	v_fma_f32 v92, v12, v92, v245
	v_fma_f32 v93, v12, v93, v248
	v_fma_f32 v94, v12, v94, v251
	v_fma_f32 v95, v12, v95, v254
	v_fma_f32 v88, 2.0, v244, v84
	v_fma_f32 v89, 2.0, v247, v85
	v_fma_f32 v90, 2.0, v250, v86
	v_fma_f32 v91, 2.0, v253, v87
	v_sub_f32_e32 v84, v84, v245
	v_sub_f32_e32 v85, v85, v248
	v_sub_f32_e32 v86, v86, v251
	v_sub_f32_e32 v87, v87, v254
	v_fma_f32 v96, -2.0, v244, v96
	v_fma_f32 v97, -2.0, v247, v97
	v_fma_f32 v98, -2.0, v250, v98
	v_fma_f32 v99, -2.0, v253, v99
	v_mul_f32_e32 v84, v84, v92
	v_mul_f32_e32 v85, v85, v93
	v_mul_f32_e32 v86, v86, v94
	v_mul_f32_e32 v87, v87, v95
	v_rcp_f32_e32 v84, v84
	v_rcp_f32_e32 v85, v85
	v_rcp_f32_e32 v86, v86
	v_rcp_f32_e32 v87, v87
	v_mul_f32_e32 v88, v88, v96
	v_mul_f32_e32 v89, v89, v97
	v_mul_f32_e32 v90, v90, v98
	v_mul_f32_e32 v91, v91, v99
	v_fma_f32 v19, v88, v84, v19
	v_fma_f32 v20, v89, v85, v20
	v_fma_f32 v21, v90, v86, v21
	v_fma_f32 v22, v91, v87, v22
	s_waitcnt lgkmcnt(0)
	v_mfma_f32_16x16x32_f16 v[84:87], v[28:31], v[228:231], 0
	v_mfma_f32_16x16x32_f16 v[88:91], v[28:31], v[232:235], 0
	v_mfma_f32_16x16x32_f16 v[92:95], v[28:31], v[236:239], v[0:3]
	v_mfma_f32_16x16x32_f16 v[96:99], v[28:31], v[240:243], 0
	v_mfma_f32_16x16x32_f16 v[84:87], v[32:35], v[36:39], v[84:87]
	v_mfma_f32_16x16x32_f16 v[88:91], v[32:35], v[44:47], v[88:91]
	v_mfma_f32_16x16x32_f16 v[92:95], v[32:35], v[52:55], v[92:95]
	v_mfma_f32_16x16x32_f16 v[96:99], v[32:35], v[60:63], v[96:99]
	v_mul_f32_e32 v244, v68, v72
	v_mul_f32_e32 v247, v69, v73
	v_mul_f32_e32 v250, v70, v74
	v_mul_f32_e32 v253, v71, v75
	v_mul_f32_e64 v245, -v72, v72
	v_mul_f32_e64 v248, -v73, v73
	v_mul_f32_e64 v251, -v74, v74
	v_mul_f32_e64 v254, -v75, v75
	v_add_f32_e32 v246, v68, v72
	v_add_f32_e32 v249, v69, v73
	v_add_f32_e32 v252, v70, v74
	v_add_f32_e32 v255, v71, v75
	v_fma_f32 v245, -v68, v68, v245
	v_fma_f32 v248, -v69, v69, v248
	v_fma_f32 v251, -v70, v70, v251
	v_fma_f32 v254, -v71, v71, v254
	v_fma_f32 v68, v10, v246, v11
	v_fma_f32 v69, v10, v249, v11
	v_fma_f32 v70, v10, v252, v11
	v_fma_f32 v71, v10, v255, v11
	v_fma_f32 v80, v13, v80, v14
	v_fma_f32 v81, v13, v81, v14
	v_fma_f32 v82, v13, v82, v14
	v_fma_f32 v83, v13, v83, v14
	v_fma_f32 v76, v12, v76, v245
	v_fma_f32 v77, v12, v77, v248
	v_fma_f32 v78, v12, v78, v251
	v_fma_f32 v79, v12, v79, v254
	v_fma_f32 v72, 2.0, v244, v68
	v_fma_f32 v73, 2.0, v247, v69
	v_fma_f32 v74, 2.0, v250, v70
	v_fma_f32 v75, 2.0, v253, v71
	v_sub_f32_e32 v68, v68, v245
	v_sub_f32_e32 v69, v69, v248
	v_sub_f32_e32 v70, v70, v251
	v_sub_f32_e32 v71, v71, v254
	v_fma_f32 v80, -2.0, v244, v80
	v_fma_f32 v81, -2.0, v247, v81
	v_fma_f32 v82, -2.0, v250, v82
	v_fma_f32 v83, -2.0, v253, v83
	v_mul_f32_e32 v68, v68, v76
	v_mul_f32_e32 v69, v69, v77
	v_mul_f32_e32 v70, v70, v78
	v_mul_f32_e32 v71, v71, v79
	v_rcp_f32_e32 v68, v68
	v_rcp_f32_e32 v69, v69
	v_rcp_f32_e32 v70, v70
	v_rcp_f32_e32 v71, v71
	v_mul_f32_e32 v72, v72, v80
	v_mul_f32_e32 v73, v73, v81
	v_mul_f32_e32 v74, v74, v82
	v_mul_f32_e32 v75, v75, v83
	v_fma_f32 v19, v72, v68, v19
	v_fma_f32 v20, v73, v69, v20
	v_fma_f32 v21, v74, v70, v21
	v_fma_f32 v22, v75, v71, v22
	v_mul_f32_e32 v244, v84, v88
	v_mul_f32_e32 v247, v85, v89
	v_mul_f32_e32 v250, v86, v90
	v_mul_f32_e32 v253, v87, v91
	v_mul_f32_e64 v245, -v88, v88
	v_mul_f32_e64 v248, -v89, v89
	v_mul_f32_e64 v251, -v90, v90
	v_mul_f32_e64 v254, -v91, v91
	v_add_f32_e32 v246, v84, v88
	v_add_f32_e32 v249, v85, v89
	v_add_f32_e32 v252, v86, v90
	v_add_f32_e32 v255, v87, v91
	v_fma_f32 v245, -v84, v84, v245
	v_fma_f32 v248, -v85, v85, v248
	v_fma_f32 v251, -v86, v86, v251
	v_fma_f32 v254, -v87, v87, v254
	v_fma_f32 v84, v10, v246, v11
	v_fma_f32 v85, v10, v249, v11
	v_fma_f32 v86, v10, v252, v11
	v_fma_f32 v87, v10, v255, v11
	v_fma_f32 v96, v13, v96, v14
	v_fma_f32 v97, v13, v97, v14
	v_fma_f32 v98, v13, v98, v14
	v_fma_f32 v99, v13, v99, v14
	v_fma_f32 v92, v12, v92, v245
	v_fma_f32 v93, v12, v93, v248
	v_fma_f32 v94, v12, v94, v251
	v_fma_f32 v95, v12, v95, v254
	v_fma_f32 v88, 2.0, v244, v84
	v_fma_f32 v89, 2.0, v247, v85
	v_fma_f32 v90, 2.0, v250, v86
	v_fma_f32 v91, 2.0, v253, v87
	v_sub_f32_e32 v84, v84, v245
	v_sub_f32_e32 v85, v85, v248
	v_sub_f32_e32 v86, v86, v251
	v_sub_f32_e32 v87, v87, v254
	v_fma_f32 v96, -2.0, v244, v96
	v_fma_f32 v97, -2.0, v247, v97
	v_fma_f32 v98, -2.0, v250, v98
	v_fma_f32 v99, -2.0, v253, v99
	v_mul_f32_e32 v84, v84, v92
	v_mul_f32_e32 v85, v85, v93
	v_mul_f32_e32 v86, v86, v94
	v_mul_f32_e32 v87, v87, v95
	v_rcp_f32_e32 v84, v84
	v_rcp_f32_e32 v85, v85
	v_rcp_f32_e32 v86, v86
	v_rcp_f32_e32 v87, v87
	v_mul_f32_e32 v88, v88, v96
	v_mul_f32_e32 v89, v89, v97
	v_mul_f32_e32 v90, v90, v98
	v_mul_f32_e32 v91, v91, v99
	v_mul_f32_e32 v88, v88, v84
	v_mul_f32_e32 v89, v89, v85
	v_mul_f32_e32 v90, v90, v86
	v_mul_f32_e32 v91, v91, v87
	v_fma_f32 v19, v88, v15, v19
	v_fma_f32 v20, v89, v16, v20
	v_fma_f32 v21, v90, v17, v21
	v_fma_f32 v22, v91, v18, v22
	s_waitcnt vmcnt(12)
	v_cvt_pk_f16_f32 v36, v100, v104
	v_cvt_pk_f16_f32 v52, v132, v136
	v_pk_add_f16 v36, v36, -0.5 op_sel_hi:[1,0]
	v_pk_add_f16 v52, v52, -0.5 op_sel_hi:[1,0]
	v_pk_mul_f16 v68, v52, v52
	v_pk_mul_f16 v84, v36, v52
	v_pk_fma_f16 v68, v36, v36, v68
	v_cvt_pk_f16_f32 v40, v101, v105
	v_cvt_pk_f16_f32 v56, v133, v137
	v_pk_add_f16 v40, v40, -0.5 op_sel_hi:[1,0]
	v_pk_add_f16 v56, v56, -0.5 op_sel_hi:[1,0]
	v_pk_mul_f16 v72, v56, v56
	v_pk_mul_f16 v88, v40, v56
	v_pk_fma_f16 v72, v40, v40, v72
	v_cvt_pk_f16_f32 v44, v102, v106
	v_cvt_pk_f16_f32 v60, v134, v138
	v_pk_add_f16 v44, v44, -0.5 op_sel_hi:[1,0]
	v_pk_add_f16 v60, v60, -0.5 op_sel_hi:[1,0]
	v_pk_mul_f16 v76, v60, v60
	v_pk_mul_f16 v92, v44, v60
	v_pk_fma_f16 v76, v44, v44, v76
	v_cvt_pk_f16_f32 v48, v103, v107
	v_cvt_pk_f16_f32 v64, v135, v139
	v_pk_add_f16 v48, v48, -0.5 op_sel_hi:[1,0]
	v_pk_add_f16 v64, v64, -0.5 op_sel_hi:[1,0]
	v_pk_mul_f16 v80, v64, v64
	v_pk_mul_f16 v96, v48, v64
	v_pk_fma_f16 v80, v48, v48, v80
	s_waitcnt vmcnt(8)
	v_cvt_pk_f16_f32 v37, v108, v112
	v_cvt_pk_f16_f32 v53, v140, v144
	v_pk_add_f16 v37, v37, -0.5 op_sel_hi:[1,0]
	v_pk_add_f16 v53, v53, -0.5 op_sel_hi:[1,0]
	v_pk_mul_f16 v69, v53, v53
	v_pk_mul_f16 v85, v37, v53
	v_pk_fma_f16 v69, v37, v37, v69
	v_cvt_pk_f16_f32 v41, v109, v113
	v_cvt_pk_f16_f32 v57, v141, v145
	v_pk_add_f16 v41, v41, -0.5 op_sel_hi:[1,0]
	v_pk_add_f16 v57, v57, -0.5 op_sel_hi:[1,0]
	v_pk_mul_f16 v73, v57, v57
	v_pk_mul_f16 v89, v41, v57
	v_pk_fma_f16 v73, v41, v41, v73
	v_cvt_pk_f16_f32 v45, v110, v114
	v_cvt_pk_f16_f32 v61, v142, v146
	v_pk_add_f16 v45, v45, -0.5 op_sel_hi:[1,0]
	v_pk_add_f16 v61, v61, -0.5 op_sel_hi:[1,0]
	v_pk_mul_f16 v77, v61, v61
	v_pk_mul_f16 v93, v45, v61
	v_pk_fma_f16 v77, v45, v45, v77
	v_cvt_pk_f16_f32 v49, v111, v115
	v_cvt_pk_f16_f32 v65, v143, v147
	v_pk_add_f16 v49, v49, -0.5 op_sel_hi:[1,0]
	v_pk_add_f16 v65, v65, -0.5 op_sel_hi:[1,0]
	v_pk_mul_f16 v81, v65, v65
	v_pk_mul_f16 v97, v49, v65
	v_pk_fma_f16 v81, v49, v49, v81
	s_waitcnt vmcnt(4)
	v_cvt_pk_f16_f32 v38, v116, v120
	v_cvt_pk_f16_f32 v54, v148, v152
	v_pk_add_f16 v38, v38, -0.5 op_sel_hi:[1,0]
	v_pk_add_f16 v54, v54, -0.5 op_sel_hi:[1,0]
	v_pk_mul_f16 v70, v54, v54
	v_pk_mul_f16 v86, v38, v54
	v_pk_fma_f16 v70, v38, v38, v70
	v_cvt_pk_f16_f32 v42, v117, v121
	v_cvt_pk_f16_f32 v58, v149, v153
	v_pk_add_f16 v42, v42, -0.5 op_sel_hi:[1,0]
	v_pk_add_f16 v58, v58, -0.5 op_sel_hi:[1,0]
	v_pk_mul_f16 v74, v58, v58
	v_pk_mul_f16 v90, v42, v58
	v_pk_fma_f16 v74, v42, v42, v74
	v_cvt_pk_f16_f32 v46, v118, v122
	v_cvt_pk_f16_f32 v62, v150, v154
	v_pk_add_f16 v46, v46, -0.5 op_sel_hi:[1,0]
	v_pk_add_f16 v62, v62, -0.5 op_sel_hi:[1,0]
	v_pk_mul_f16 v78, v62, v62
	v_pk_mul_f16 v94, v46, v62
	v_pk_fma_f16 v78, v46, v46, v78
	v_cvt_pk_f16_f32 v50, v119, v123
	v_cvt_pk_f16_f32 v66, v151, v155
	v_pk_add_f16 v50, v50, -0.5 op_sel_hi:[1,0]
	v_pk_add_f16 v66, v66, -0.5 op_sel_hi:[1,0]
	v_pk_mul_f16 v82, v66, v66
	v_pk_mul_f16 v98, v50, v66
	v_pk_fma_f16 v82, v50, v50, v82
	s_waitcnt vmcnt(0)
	v_cvt_pk_f16_f32 v39, v124, v128
	v_cvt_pk_f16_f32 v55, v156, v160
	v_pk_add_f16 v39, v39, -0.5 op_sel_hi:[1,0]
	v_pk_add_f16 v55, v55, -0.5 op_sel_hi:[1,0]
	v_pk_mul_f16 v71, v55, v55
	v_pk_mul_f16 v87, v39, v55
	v_pk_fma_f16 v71, v39, v39, v71
	v_cvt_pk_f16_f32 v43, v125, v129
	v_cvt_pk_f16_f32 v59, v157, v161
	v_pk_add_f16 v43, v43, -0.5 op_sel_hi:[1,0]
	v_pk_add_f16 v59, v59, -0.5 op_sel_hi:[1,0]
	v_pk_mul_f16 v75, v59, v59
	v_pk_mul_f16 v91, v43, v59
	v_pk_fma_f16 v75, v43, v43, v75
	v_cvt_pk_f16_f32 v47, v126, v130
	v_cvt_pk_f16_f32 v63, v158, v162
	v_pk_add_f16 v47, v47, -0.5 op_sel_hi:[1,0]
	v_pk_add_f16 v63, v63, -0.5 op_sel_hi:[1,0]
	v_pk_mul_f16 v79, v63, v63
	v_pk_mul_f16 v95, v47, v63
	v_pk_fma_f16 v79, v47, v47, v79
	v_cvt_pk_f16_f32 v51, v127, v131
	v_cvt_pk_f16_f32 v67, v159, v163
	v_pk_add_f16 v51, v51, -0.5 op_sel_hi:[1,0]
	v_pk_add_f16 v67, v67, -0.5 op_sel_hi:[1,0]
	v_pk_mul_f16 v83, v67, v67
	v_pk_mul_f16 v99, v51, v67
	v_pk_fma_f16 v83, v51, v51, v83
	v_mfma_f32_16x16x32_f16 v[132:135], v[164:167], v[28:31], 0
	v_mfma_f32_16x16x32_f16 v[136:139], v[168:171], v[28:31], 0
	v_mfma_f32_16x16x32_f16 v[140:143], v[172:175], v[28:31], 0
	v_mfma_f32_16x16x32_f16 v[144:147], v[176:179], v[28:31], 0
	v_mfma_f32_16x16x32_f16 v[132:135], v[36:39], v[32:35], v[132:135]
	v_mfma_f32_16x16x32_f16 v[136:139], v[40:43], v[32:35], v[136:139]
	v_mfma_f32_16x16x32_f16 v[140:143], v[44:47], v[32:35], v[140:143]
	v_mfma_f32_16x16x32_f16 v[144:147], v[48:51], v[32:35], v[144:147]
	v_mfma_f32_16x16x32_f16 v[148:151], v[180:183], v[28:31], 0
	v_mfma_f32_16x16x32_f16 v[152:155], v[184:187], v[28:31], 0
	v_mfma_f32_16x16x32_f16 v[156:159], v[188:191], v[28:31], 0
	v_mfma_f32_16x16x32_f16 v[160:163], v[192:195], v[28:31], 0
	v_mfma_f32_16x16x32_f16 v[148:151], v[52:55], v[32:35], v[148:151]
	v_mfma_f32_16x16x32_f16 v[152:155], v[56:59], v[32:35], v[152:155]
	v_mfma_f32_16x16x32_f16 v[156:159], v[60:63], v[32:35], v[156:159]
	v_mfma_f32_16x16x32_f16 v[160:163], v[64:67], v[32:35], v[160:163]
	v_cvt_pk_f16_f32 v100, v132, v136
	v_cvt_pk_f16_f32 v101, v140, v144
	v_cvt_pk_f16_f32 v102, v133, v137
	v_cvt_pk_f16_f32 v103, v141, v145
	v_cvt_pk_f16_f32 v104, v134, v138
	v_cvt_pk_f16_f32 v105, v142, v146
	v_cvt_pk_f16_f32 v106, v135, v139
	v_cvt_pk_f16_f32 v107, v143, v147
	v_mfma_f32_16x16x32_f16 v[132:135], v[196:199], v[28:31], 0
	v_mfma_f32_16x16x32_f16 v[136:139], v[200:203], v[28:31], 0
	v_mfma_f32_16x16x32_f16 v[140:143], v[204:207], v[28:31], 0
	v_mfma_f32_16x16x32_f16 v[144:147], v[208:211], v[28:31], 0
	v_mfma_f32_16x16x32_f16 v[132:135], v[68:71], v[32:35], v[132:135]
	v_mfma_f32_16x16x32_f16 v[136:139], v[72:75], v[32:35], v[136:139]
	v_mfma_f32_16x16x32_f16 v[140:143], v[76:79], v[32:35], v[140:143]
	v_mfma_f32_16x16x32_f16 v[144:147], v[80:83], v[32:35], v[144:147]
	v_cvt_pk_f16_f32 v108, v148, v152
	v_cvt_pk_f16_f32 v109, v156, v160
	v_cvt_pk_f16_f32 v110, v149, v153
	v_cvt_pk_f16_f32 v111, v157, v161
	v_cvt_pk_f16_f32 v112, v150, v154
	v_cvt_pk_f16_f32 v113, v158, v162
	v_cvt_pk_f16_f32 v114, v151, v155
	v_cvt_pk_f16_f32 v115, v159, v163
	v_mfma_f32_16x16x32_f16 v[148:151], v[212:215], v[28:31], 0
	v_mfma_f32_16x16x32_f16 v[152:155], v[216:219], v[28:31], 0
	v_mfma_f32_16x16x32_f16 v[156:159], v[220:223], v[28:31], 0
	v_mfma_f32_16x16x32_f16 v[160:163], v[224:227], v[28:31], 0
	v_mfma_f32_16x16x32_f16 v[148:151], v[84:87], v[32:35], v[148:151]
	v_mfma_f32_16x16x32_f16 v[152:155], v[88:91], v[32:35], v[152:155]
	v_mfma_f32_16x16x32_f16 v[156:159], v[92:95], v[32:35], v[156:159]
	v_mfma_f32_16x16x32_f16 v[160:163], v[96:99], v[32:35], v[160:163]
	v_cvt_pk_f16_f32 v116, v132, v136
	v_cvt_pk_f16_f32 v117, v140, v144
	v_cvt_pk_f16_f32 v118, v133, v137
	v_cvt_pk_f16_f32 v119, v141, v145
	v_cvt_pk_f16_f32 v120, v134, v138
	v_cvt_pk_f16_f32 v121, v142, v146
	v_cvt_pk_f16_f32 v122, v135, v139
	v_cvt_pk_f16_f32 v123, v143, v147
	v_cvt_pk_f16_f32 v124, v148, v152
	v_cvt_pk_f16_f32 v125, v156, v160
	v_cvt_pk_f16_f32 v126, v149, v153
	v_cvt_pk_f16_f32 v127, v157, v161
	v_cvt_pk_f16_f32 v128, v150, v154
	v_cvt_pk_f16_f32 v129, v158, v162
	v_cvt_pk_f16_f32 v130, v151, v155
	v_cvt_pk_f16_f32 v131, v159, v163
	global_load_dwordx4 v[164:167], v23, s[84:85] offset:0 sc1 nt
	global_load_dwordx4 v[168:171], v23, s[84:85] offset:2048 sc1 nt
	global_load_dwordx4 v[180:183], v23, s[88:89] offset:0 sc1 nt
	global_load_dwordx4 v[184:187], v23, s[88:89] offset:2048 sc1 nt
	global_load_dwordx4 v[172:175], v23, s[86:87] offset:0 sc1 nt
	global_load_dwordx4 v[176:179], v23, s[86:87] offset:2048 sc1 nt
	global_load_dwordx4 v[188:191], v23, s[90:91] offset:0 sc1 nt
	global_load_dwordx4 v[192:195], v23, s[90:91] offset:2048 sc1 nt
	s_mov_b64 exec, s[38:39]
	ds_write_b128 v4, v[104:107] offset:16384
	ds_write_b128 v4, v[112:115] offset:16896
	ds_write_b128 v4, v[120:123] offset:17408
	ds_write_b128 v4, v[128:131] offset:17920
	s_mov_b64 exec, -1
	v_mfma_f32_16x16x32_f16 v[132:135], v[24:27], v[100:103], 0
	v_mfma_f32_16x16x32_f16 v[136:139], v[24:27], v[108:111], 0
	v_mfma_f32_16x16x32_f16 v[140:143], v[24:27], v[116:119], v[0:3]
	v_mfma_f32_16x16x32_f16 v[144:147], v[24:27], v[124:127], 0
	v_mfma_f32_16x16x32_f16 v[148:151], v[28:31], v[100:103], 0
	v_mfma_f32_16x16x32_f16 v[152:155], v[28:31], v[108:111], 0
	v_mfma_f32_16x16x32_f16 v[156:159], v[28:31], v[116:119], v[0:3]
	v_mfma_f32_16x16x32_f16 v[160:163], v[28:31], v[124:127], 0
	v_mfma_f32_16x16x32_f16 v[148:151], v[32:35], v[104:107], v[148:151]
	v_mfma_f32_16x16x32_f16 v[152:155], v[32:35], v[112:115], v[152:155]
	v_mfma_f32_16x16x32_f16 v[156:159], v[32:35], v[120:123], v[156:159]
	v_mfma_f32_16x16x32_f16 v[160:163], v[32:35], v[128:131], v[160:163]
	s_waitcnt lgkmcnt(0)
	ds_write_b32 v6, v6 offset:32
	ds_read_b32 v9, v7 offset:32
	v_mul_f32_e32 v244, v132, v136
	v_mul_f32_e32 v247, v133, v137
	v_mul_f32_e32 v250, v134, v138
	v_mul_f32_e32 v253, v135, v139
	v_mul_f32_e64 v245, -v136, v136
	v_mul_f32_e64 v248, -v137, v137
	v_mul_f32_e64 v251, -v138, v138
	v_mul_f32_e64 v254, -v139, v139
	v_add_f32_e32 v246, v132, v136
	v_add_f32_e32 v249, v133, v137
	v_add_f32_e32 v252, v134, v138
	v_add_f32_e32 v255, v135, v139
	v_fma_f32 v245, -v132, v132, v245
	v_fma_f32 v248, -v133, v133, v248
	v_fma_f32 v251, -v134, v134, v251
	v_fma_f32 v254, -v135, v135, v254
	v_fma_f32 v132, v10, v246, v11
	v_fma_f32 v133, v10, v249, v11
	v_fma_f32 v134, v10, v252, v11
	v_fma_f32 v135, v10, v255, v11
	v_fma_f32 v144, v13, v144, v14
	v_fma_f32 v145, v13, v145, v14
	v_fma_f32 v146, v13, v146, v14
	v_fma_f32 v147, v13, v147, v14
	v_fma_f32 v140, v12, v140, v245
	v_fma_f32 v141, v12, v141, v248
	v_fma_f32 v142, v12, v142, v251
	v_fma_f32 v143, v12, v143, v254
	v_fma_f32 v136, 2.0, v244, v132
	v_fma_f32 v137, 2.0, v247, v133
	v_fma_f32 v138, 2.0, v250, v134
	v_fma_f32 v139, 2.0, v253, v135
	v_sub_f32_e32 v132, v132, v245
	v_sub_f32_e32 v133, v133, v248
	v_sub_f32_e32 v134, v134, v251
	v_sub_f32_e32 v135, v135, v254
	v_fma_f32 v144, -2.0, v244, v144
	v_fma_f32 v145, -2.0, v247, v145
	v_fma_f32 v146, -2.0, v250, v146
	v_fma_f32 v147, -2.0, v253, v147
	v_mul_f32_e32 v132, v132, v140
	v_mul_f32_e32 v133, v133, v141
	v_mul_f32_e32 v134, v134, v142
	v_mul_f32_e32 v135, v135, v143
	v_rcp_f32_e32 v132, v132
	v_rcp_f32_e32 v133, v133
	v_rcp_f32_e32 v134, v134
	v_rcp_f32_e32 v135, v135
	v_mul_f32_e32 v136, v136, v144
	v_mul_f32_e32 v137, v137, v145
	v_mul_f32_e32 v138, v138, v146
	v_mul_f32_e32 v139, v139, v147
	v_fma_f32 v19, v136, v132, v19
	v_fma_f32 v20, v137, v133, v20
	v_fma_f32 v21, v138, v134, v21
	v_fma_f32 v22, v139, v135, v22
	v_mfma_f32_16x16x32_f16 v[132:135], v[24:27], v[104:107], 0
	v_mfma_f32_16x16x32_f16 v[136:139], v[24:27], v[112:115], 0
	v_mfma_f32_16x16x32_f16 v[140:143], v[24:27], v[120:123], v[0:3]
	v_mfma_f32_16x16x32_f16 v[144:147], v[24:27], v[128:131], 0
	s_waitcnt lgkmcnt(0)
	v_cmp_ne_u32_e32 vcc, 0, v9
	s_cbranch_vccnz .Lq_go_1

.Lq_go_1:
	ds_read_b128 v[228:231], v5 offset:16384
	ds_read_b128 v[232:235], v5 offset:16896
	ds_read_b128 v[236:239], v5 offset:17408
	ds_read_b128 v[240:243], v5 offset:17920
	v_mul_f32_e32 v244, v148, v152
	v_mul_f32_e32 v247, v149, v153
	v_mul_f32_e32 v250, v150, v154
	v_mul_f32_e32 v253, v151, v155
	v_mul_f32_e64 v245, -v152, v152
	v_mul_f32_e64 v248, -v153, v153
	v_mul_f32_e64 v251, -v154, v154
	v_mul_f32_e64 v254, -v155, v155
	v_add_f32_e32 v246, v148, v152
	v_add_f32_e32 v249, v149, v153
	v_add_f32_e32 v252, v150, v154
	v_add_f32_e32 v255, v151, v155
	v_fma_f32 v245, -v148, v148, v245
	v_fma_f32 v248, -v149, v149, v248
	v_fma_f32 v251, -v150, v150, v251
	v_fma_f32 v254, -v151, v151, v254
	v_fma_f32 v148, v10, v246, v11
	v_fma_f32 v149, v10, v249, v11
	v_fma_f32 v150, v10, v252, v11
	v_fma_f32 v151, v10, v255, v11
	v_fma_f32 v160, v13, v160, v14
	v_fma_f32 v161, v13, v161, v14
	v_fma_f32 v162, v13, v162, v14
	v_fma_f32 v163, v13, v163, v14
	v_fma_f32 v156, v12, v156, v245
	v_fma_f32 v157, v12, v157, v248
	v_fma_f32 v158, v12, v158, v251
	v_fma_f32 v159, v12, v159, v254
	v_fma_f32 v152, 2.0, v244, v148
	v_fma_f32 v153, 2.0, v247, v149
	v_fma_f32 v154, 2.0, v250, v150
	v_fma_f32 v155, 2.0, v253, v151
	v_sub_f32_e32 v148, v148, v245
	v_sub_f32_e32 v149, v149, v248
	v_sub_f32_e32 v150, v150, v251
	v_sub_f32_e32 v151, v151, v254
	v_fma_f32 v160, -2.0, v244, v160
	v_fma_f32 v161, -2.0, v247, v161
	v_fma_f32 v162, -2.0, v250, v162
	v_fma_f32 v163, -2.0, v253, v163
	v_mul_f32_e32 v148, v148, v156
	v_mul_f32_e32 v149, v149, v157
	v_mul_f32_e32 v150, v150, v158
	v_mul_f32_e32 v151, v151, v159
	v_rcp_f32_e32 v148, v148
	v_rcp_f32_e32 v149, v149
	v_rcp_f32_e32 v150, v150
	v_rcp_f32_e32 v151, v151
	v_mul_f32_e32 v152, v152, v160
	v_mul_f32_e32 v153, v153, v161
	v_mul_f32_e32 v154, v154, v162
	v_mul_f32_e32 v155, v155, v163
	v_fma_f32 v19, v152, v148, v19
	v_fma_f32 v20, v153, v149, v20
	v_fma_f32 v21, v154, v150, v21
	v_fma_f32 v22, v155, v151, v22
	s_waitcnt lgkmcnt(0)
	v_mfma_f32_16x16x32_f16 v[148:151], v[28:31], v[228:231], 0
	v_mfma_f32_16x16x32_f16 v[152:155], v[28:31], v[232:235], 0
	v_mfma_f32_16x16x32_f16 v[156:159], v[28:31], v[236:239], v[0:3]
	v_mfma_f32_16x16x32_f16 v[160:163], v[28:31], v[240:243], 0
	v_mfma_f32_16x16x32_f16 v[148:151], v[32:35], v[100:103], v[148:151]
	v_mfma_f32_16x16x32_f16 v[152:155], v[32:35], v[108:111], v[152:155]
	v_mfma_f32_16x16x32_f16 v[156:159], v[32:35], v[116:119], v[156:159]
	v_mfma_f32_16x16x32_f16 v[160:163], v[32:35], v[124:127], v[160:163]
	v_mul_f32_e32 v244, v132, v136
	v_mul_f32_e32 v247, v133, v137
	v_mul_f32_e32 v250, v134, v138
	v_mul_f32_e32 v253, v135, v139
	v_mul_f32_e64 v245, -v136, v136
	v_mul_f32_e64 v248, -v137, v137
	v_mul_f32_e64 v251, -v138, v138
	v_mul_f32_e64 v254, -v139, v139
	v_add_f32_e32 v246, v132, v136
	v_add_f32_e32 v249, v133, v137
	v_add_f32_e32 v252, v134, v138
	v_add_f32_e32 v255, v135, v139
	v_fma_f32 v245, -v132, v132, v245
	v_fma_f32 v248, -v133, v133, v248
	v_fma_f32 v251, -v134, v134, v251
	v_fma_f32 v254, -v135, v135, v254
	v_fma_f32 v132, v10, v246, v11
	v_fma_f32 v133, v10, v249, v11
	v_fma_f32 v134, v10, v252, v11
	v_fma_f32 v135, v10, v255, v11
	v_fma_f32 v144, v13, v144, v14
	v_fma_f32 v145, v13, v145, v14
	v_fma_f32 v146, v13, v146, v14
	v_fma_f32 v147, v13, v147, v14
	v_fma_f32 v140, v12, v140, v245
	v_fma_f32 v141, v12, v141, v248
	v_fma_f32 v142, v12, v142, v251
	v_fma_f32 v143, v12, v143, v254
	v_fma_f32 v136, 2.0, v244, v132
	v_fma_f32 v137, 2.0, v247, v133
	v_fma_f32 v138, 2.0, v250, v134
	v_fma_f32 v139, 2.0, v253, v135
	v_sub_f32_e32 v132, v132, v245
	v_sub_f32_e32 v133, v133, v248
	v_sub_f32_e32 v134, v134, v251
	v_sub_f32_e32 v135, v135, v254
	v_fma_f32 v144, -2.0, v244, v144
	v_fma_f32 v145, -2.0, v247, v145
	v_fma_f32 v146, -2.0, v250, v146
	v_fma_f32 v147, -2.0, v253, v147
	v_mul_f32_e32 v132, v132, v140
	v_mul_f32_e32 v133, v133, v141
	v_mul_f32_e32 v134, v134, v142
	v_mul_f32_e32 v135, v135, v143
	v_rcp_f32_e32 v132, v132
	v_rcp_f32_e32 v133, v133
	v_rcp_f32_e32 v134, v134
	v_rcp_f32_e32 v135, v135
	v_mul_f32_e32 v136, v136, v144
	v_mul_f32_e32 v137, v137, v145
	v_mul_f32_e32 v138, v138, v146
	v_mul_f32_e32 v139, v139, v147
	v_fma_f32 v19, v136, v132, v19
	v_fma_f32 v20, v137, v133, v20
	v_fma_f32 v21, v138, v134, v21
	v_fma_f32 v22, v139, v135, v22
	v_mul_f32_e32 v244, v148, v152
	v_mul_f32_e32 v247, v149, v153
	v_mul_f32_e32 v250, v150, v154
	v_mul_f32_e32 v253, v151, v155
	v_mul_f32_e64 v245, -v152, v152
	v_mul_f32_e64 v248, -v153, v153
	v_mul_f32_e64 v251, -v154, v154
	v_mul_f32_e64 v254, -v155, v155
	v_add_f32_e32 v246, v148, v152
	v_add_f32_e32 v249, v149, v153
	v_add_f32_e32 v252, v150, v154
	v_add_f32_e32 v255, v151, v155
	v_fma_f32 v245, -v148, v148, v245
	v_fma_f32 v248, -v149, v149, v248
	v_fma_f32 v251, -v150, v150, v251
	v_fma_f32 v254, -v151, v151, v254
	v_fma_f32 v148, v10, v246, v11
	v_fma_f32 v149, v10, v249, v11
	v_fma_f32 v150, v10, v252, v11
	v_fma_f32 v151, v10, v255, v11
	v_fma_f32 v160, v13, v160, v14
	v_fma_f32 v161, v13, v161, v14
	v_fma_f32 v162, v13, v162, v14
	v_fma_f32 v163, v13, v163, v14
	v_fma_f32 v156, v12, v156, v245
	v_fma_f32 v157, v12, v157, v248
	v_fma_f32 v158, v12, v158, v251
	v_fma_f32 v159, v12, v159, v254
	v_fma_f32 v152, 2.0, v244, v148
	v_fma_f32 v153, 2.0, v247, v149
	v_fma_f32 v154, 2.0, v250, v150
	v_fma_f32 v155, 2.0, v253, v151
	v_sub_f32_e32 v148, v148, v245
	v_sub_f32_e32 v149, v149, v248
	v_sub_f32_e32 v150, v150, v251
	v_sub_f32_e32 v151, v151, v254
	v_fma_f32 v160, -2.0, v244, v160
	v_fma_f32 v161, -2.0, v247, v161
	v_fma_f32 v162, -2.0, v250, v162
	v_fma_f32 v163, -2.0, v253, v163
	v_mul_f32_e32 v148, v148, v156
	v_mul_f32_e32 v149, v149, v157
	v_mul_f32_e32 v150, v150, v158
	v_mul_f32_e32 v151, v151, v159
	v_rcp_f32_e32 v148, v148
	v_rcp_f32_e32 v149, v149
	v_rcp_f32_e32 v150, v150
	v_rcp_f32_e32 v151, v151
	v_mul_f32_e32 v152, v152, v160
	v_mul_f32_e32 v153, v153, v161
	v_mul_f32_e32 v154, v154, v162
	v_mul_f32_e32 v155, v155, v163
	v_mul_f32_e32 v152, v152, v148
	v_mul_f32_e32 v153, v153, v149
	v_mul_f32_e32 v154, v154, v150
	v_mul_f32_e32 v155, v155, v151
	v_fma_f32 v19, v152, v15, v19
	v_fma_f32 v20, v153, v16, v20
	v_fma_f32 v21, v154, v17, v21
	v_fma_f32 v22, v155, v18, v22
	v_mfma_f32_16x16x32_f16 v[132:135], v[36:39], v[24:27], 0
	v_mfma_f32_16x16x32_f16 v[136:139], v[40:43], v[24:27], 0
	v_mfma_f32_16x16x32_f16 v[140:143], v[44:47], v[24:27], 0
	v_mfma_f32_16x16x32_f16 v[144:147], v[48:51], v[24:27], 0
	v_mfma_f32_16x16x32_f16 v[148:151], v[52:55], v[24:27], 0
	v_mfma_f32_16x16x32_f16 v[152:155], v[56:59], v[24:27], 0
	v_mfma_f32_16x16x32_f16 v[156:159], v[60:63], v[24:27], 0
	v_mfma_f32_16x16x32_f16 v[160:163], v[64:67], v[24:27], 0
	s_nop 1
	v_cvt_pk_f16_f32 v100, v132, v136
	s_nop 0
	v_cvt_pk_f16_f32 v101, v140, v144
	v_cvt_pk_f16_f32 v102, v133, v137
	v_cvt_pk_f16_f32 v103, v141, v145
	v_cvt_pk_f16_f32 v104, v134, v138
	v_cvt_pk_f16_f32 v105, v142, v146
	v_cvt_pk_f16_f32 v106, v135, v139
	v_cvt_pk_f16_f32 v107, v143, v147
	v_mfma_f32_16x16x32_f16 v[132:135], v[68:71], v[24:27], 0
	v_mfma_f32_16x16x32_f16 v[136:139], v[72:75], v[24:27], 0
	v_mfma_f32_16x16x32_f16 v[140:143], v[76:79], v[24:27], 0
	v_mfma_f32_16x16x32_f16 v[144:147], v[80:83], v[24:27], 0
	v_cvt_pk_f16_f32 v108, v148, v152
	v_cvt_pk_f16_f32 v109, v156, v160
	v_cvt_pk_f16_f32 v110, v149, v153
	v_cvt_pk_f16_f32 v111, v157, v161
	v_cvt_pk_f16_f32 v112, v150, v154
	v_cvt_pk_f16_f32 v113, v158, v162
	v_cvt_pk_f16_f32 v114, v151, v155
	v_cvt_pk_f16_f32 v115, v159, v163
	v_mfma_f32_16x16x32_f16 v[148:151], v[84:87], v[24:27], 0
	v_mfma_f32_16x16x32_f16 v[152:155], v[88:91], v[24:27], 0
	v_mfma_f32_16x16x32_f16 v[156:159], v[92:95], v[24:27], 0
	v_mfma_f32_16x16x32_f16 v[160:163], v[96:99], v[24:27], 0
	v_cvt_pk_f16_f32 v116, v132, v136
	v_cvt_pk_f16_f32 v117, v140, v144
	v_cvt_pk_f16_f32 v118, v133, v137
	v_cvt_pk_f16_f32 v119, v141, v145
	v_cvt_pk_f16_f32 v120, v134, v138
	v_cvt_pk_f16_f32 v121, v142, v146
	v_cvt_pk_f16_f32 v122, v135, v139
	v_cvt_pk_f16_f32 v123, v143, v147
	v_cvt_pk_f16_f32 v124, v148, v152
	v_cvt_pk_f16_f32 v125, v156, v160
	v_cvt_pk_f16_f32 v126, v149, v153
	v_cvt_pk_f16_f32 v127, v157, v161
	v_cvt_pk_f16_f32 v128, v150, v154
	v_cvt_pk_f16_f32 v129, v158, v162
	v_cvt_pk_f16_f32 v130, v151, v155
	v_cvt_pk_f16_f32 v131, v159, v163
	s_mov_b64 exec, s[38:39]
	ds_write_b128 v4, v[104:107] offset:32768
	ds_write_b128 v4, v[112:115] offset:33280
	ds_write_b128 v4, v[120:123] offset:33792
	ds_write_b128 v4, v[128:131] offset:34304
	s_mov_b64 exec, -1
	v_mfma_f32_16x16x32_f16 v[132:135], v[24:27], v[100:103], 0
	v_mfma_f32_16x16x32_f16 v[136:139], v[24:27], v[108:111], 0
	v_mfma_f32_16x16x32_f16 v[140:143], v[24:27], v[116:119], v[0:3]
	v_mfma_f32_16x16x32_f16 v[144:147], v[24:27], v[124:127], 0
	v_mfma_f32_16x16x32_f16 v[148:151], v[28:31], v[100:103], 0
	v_mfma_f32_16x16x32_f16 v[152:155], v[28:31], v[108:111], 0
	v_mfma_f32_16x16x32_f16 v[156:159], v[28:31], v[116:119], v[0:3]
	v_mfma_f32_16x16x32_f16 v[160:163], v[28:31], v[124:127], 0
	v_mfma_f32_16x16x32_f16 v[148:151], v[32:35], v[104:107], v[148:151]
	v_mfma_f32_16x16x32_f16 v[152:155], v[32:35], v[112:115], v[152:155]
	v_mfma_f32_16x16x32_f16 v[156:159], v[32:35], v[120:123], v[156:159]
	v_mfma_f32_16x16x32_f16 v[160:163], v[32:35], v[128:131], v[160:163]
	s_waitcnt lgkmcnt(0)
	ds_write_b32 v6, v6 offset:64
	ds_read_b32 v9, v7 offset:64
	v_mul_f32_e32 v244, v132, v136
	v_mul_f32_e32 v247, v133, v137
	v_mul_f32_e32 v250, v134, v138
	v_mul_f32_e32 v253, v135, v139
	v_mul_f32_e64 v245, -v136, v136
	v_mul_f32_e64 v248, -v137, v137
	v_mul_f32_e64 v251, -v138, v138
	v_mul_f32_e64 v254, -v139, v139
	v_add_f32_e32 v246, v132, v136
	v_add_f32_e32 v249, v133, v137
	v_add_f32_e32 v252, v134, v138
	v_add_f32_e32 v255, v135, v139
	v_fma_f32 v245, -v132, v132, v245
	v_fma_f32 v248, -v133, v133, v248
	v_fma_f32 v251, -v134, v134, v251
	v_fma_f32 v254, -v135, v135, v254
	v_fma_f32 v132, v10, v246, v11
	v_fma_f32 v133, v10, v249, v11
	v_fma_f32 v134, v10, v252, v11
	v_fma_f32 v135, v10, v255, v11
	v_fma_f32 v144, v13, v144, v14
	v_fma_f32 v145, v13, v145, v14
	v_fma_f32 v146, v13, v146, v14
	v_fma_f32 v147, v13, v147, v14
	v_fma_f32 v140, v12, v140, v245
	v_fma_f32 v141, v12, v141, v248
	v_fma_f32 v142, v12, v142, v251
	v_fma_f32 v143, v12, v143, v254
	v_fma_f32 v136, 2.0, v244, v132
	v_fma_f32 v137, 2.0, v247, v133
	v_fma_f32 v138, 2.0, v250, v134
	v_fma_f32 v139, 2.0, v253, v135
	v_sub_f32_e32 v132, v132, v245
	v_sub_f32_e32 v133, v133, v248
	v_sub_f32_e32 v134, v134, v251
	v_sub_f32_e32 v135, v135, v254
	v_fma_f32 v144, -2.0, v244, v144
	v_fma_f32 v145, -2.0, v247, v145
	v_fma_f32 v146, -2.0, v250, v146
	v_fma_f32 v147, -2.0, v253, v147
	v_mul_f32_e32 v132, v132, v140
	v_mul_f32_e32 v133, v133, v141
	v_mul_f32_e32 v134, v134, v142
	v_mul_f32_e32 v135, v135, v143
	v_rcp_f32_e32 v132, v132
	v_rcp_f32_e32 v133, v133
	v_rcp_f32_e32 v134, v134
	v_rcp_f32_e32 v135, v135
	v_mul_f32_e32 v136, v136, v144
	v_mul_f32_e32 v137, v137, v145
	v_mul_f32_e32 v138, v138, v146
	v_mul_f32_e32 v139, v139, v147
	v_fma_f32 v19, v136, v132, v19
	v_fma_f32 v20, v137, v133, v20
	v_fma_f32 v21, v138, v134, v21
	v_fma_f32 v22, v139, v135, v22
	v_mfma_f32_16x16x32_f16 v[132:135], v[24:27], v[104:107], 0
	v_mfma_f32_16x16x32_f16 v[136:139], v[24:27], v[112:115], 0
	v_mfma_f32_16x16x32_f16 v[140:143], v[24:27], v[120:123], v[0:3]
	v_mfma_f32_16x16x32_f16 v[144:147], v[24:27], v[128:131], 0
	s_waitcnt lgkmcnt(0)
	v_cmp_ne_u32_e32 vcc, 0, v9
	s_cbranch_vccnz .Lq_go_2

.Lq_go_2:
	ds_read_b128 v[228:231], v5 offset:32768
	ds_read_b128 v[232:235], v5 offset:33280
	ds_read_b128 v[236:239], v5 offset:33792
	ds_read_b128 v[240:243], v5 offset:34304
	v_mul_f32_e32 v244, v148, v152
	v_mul_f32_e32 v247, v149, v153
	v_mul_f32_e32 v250, v150, v154
	v_mul_f32_e32 v253, v151, v155
	v_mul_f32_e64 v245, -v152, v152
	v_mul_f32_e64 v248, -v153, v153
	v_mul_f32_e64 v251, -v154, v154
	v_mul_f32_e64 v254, -v155, v155
	v_add_f32_e32 v246, v148, v152
	v_add_f32_e32 v249, v149, v153
	v_add_f32_e32 v252, v150, v154
	v_add_f32_e32 v255, v151, v155
	v_fma_f32 v245, -v148, v148, v245
	v_fma_f32 v248, -v149, v149, v248
	v_fma_f32 v251, -v150, v150, v251
	v_fma_f32 v254, -v151, v151, v254
	v_fma_f32 v148, v10, v246, v11
	v_fma_f32 v149, v10, v249, v11
	v_fma_f32 v150, v10, v252, v11
	v_fma_f32 v151, v10, v255, v11
	v_fma_f32 v160, v13, v160, v14
	v_fma_f32 v161, v13, v161, v14
	v_fma_f32 v162, v13, v162, v14
	v_fma_f32 v163, v13, v163, v14
	v_fma_f32 v156, v12, v156, v245
	v_fma_f32 v157, v12, v157, v248
	v_fma_f32 v158, v12, v158, v251
	v_fma_f32 v159, v12, v159, v254
	v_fma_f32 v152, 2.0, v244, v148
	v_fma_f32 v153, 2.0, v247, v149
	v_fma_f32 v154, 2.0, v250, v150
	v_fma_f32 v155, 2.0, v253, v151
	v_sub_f32_e32 v148, v148, v245
	v_sub_f32_e32 v149, v149, v248
	v_sub_f32_e32 v150, v150, v251
	v_sub_f32_e32 v151, v151, v254
	v_fma_f32 v160, -2.0, v244, v160
	v_fma_f32 v161, -2.0, v247, v161
	v_fma_f32 v162, -2.0, v250, v162
	v_fma_f32 v163, -2.0, v253, v163
	v_mul_f32_e32 v148, v148, v156
	v_mul_f32_e32 v149, v149, v157
	v_mul_f32_e32 v150, v150, v158
	v_mul_f32_e32 v151, v151, v159
	v_rcp_f32_e32 v148, v148
	v_rcp_f32_e32 v149, v149
	v_rcp_f32_e32 v150, v150
	v_rcp_f32_e32 v151, v151
	v_mul_f32_e32 v152, v152, v160
	v_mul_f32_e32 v153, v153, v161
	v_mul_f32_e32 v154, v154, v162
	v_mul_f32_e32 v155, v155, v163
	v_fma_f32 v19, v152, v148, v19
	v_fma_f32 v20, v153, v149, v20
	v_fma_f32 v21, v154, v150, v21
	v_fma_f32 v22, v155, v151, v22
	s_waitcnt lgkmcnt(0)
	v_mfma_f32_16x16x32_f16 v[148:151], v[28:31], v[228:231], 0
	v_mfma_f32_16x16x32_f16 v[152:155], v[28:31], v[232:235], 0
	v_mfma_f32_16x16x32_f16 v[156:159], v[28:31], v[236:239], v[0:3]
	v_mfma_f32_16x16x32_f16 v[160:163], v[28:31], v[240:243], 0
	v_mfma_f32_16x16x32_f16 v[148:151], v[32:35], v[100:103], v[148:151]
	v_mfma_f32_16x16x32_f16 v[152:155], v[32:35], v[108:111], v[152:155]
	v_mfma_f32_16x16x32_f16 v[156:159], v[32:35], v[116:119], v[156:159]
	v_mfma_f32_16x16x32_f16 v[160:163], v[32:35], v[124:127], v[160:163]
	v_mul_f32_e32 v244, v132, v136
	v_mul_f32_e32 v247, v133, v137
	v_mul_f32_e32 v250, v134, v138
	v_mul_f32_e32 v253, v135, v139
	v_mul_f32_e64 v245, -v136, v136
	v_mul_f32_e64 v248, -v137, v137
	v_mul_f32_e64 v251, -v138, v138
	v_mul_f32_e64 v254, -v139, v139
	v_add_f32_e32 v246, v132, v136
	v_add_f32_e32 v249, v133, v137
	v_add_f32_e32 v252, v134, v138
	v_add_f32_e32 v255, v135, v139
	v_fma_f32 v245, -v132, v132, v245
	v_fma_f32 v248, -v133, v133, v248
	v_fma_f32 v251, -v134, v134, v251
	v_fma_f32 v254, -v135, v135, v254
	v_fma_f32 v132, v10, v246, v11
	v_fma_f32 v133, v10, v249, v11
	v_fma_f32 v134, v10, v252, v11
	v_fma_f32 v135, v10, v255, v11
	v_fma_f32 v144, v13, v144, v14
	v_fma_f32 v145, v13, v145, v14
	v_fma_f32 v146, v13, v146, v14
	v_fma_f32 v147, v13, v147, v14
	v_fma_f32 v140, v12, v140, v245
	v_fma_f32 v141, v12, v141, v248
	v_fma_f32 v142, v12, v142, v251
	v_fma_f32 v143, v12, v143, v254
	v_fma_f32 v136, 2.0, v244, v132
	v_fma_f32 v137, 2.0, v247, v133
	v_fma_f32 v138, 2.0, v250, v134
	v_fma_f32 v139, 2.0, v253, v135
	v_sub_f32_e32 v132, v132, v245
	v_sub_f32_e32 v133, v133, v248
	v_sub_f32_e32 v134, v134, v251
	v_sub_f32_e32 v135, v135, v254
	v_fma_f32 v144, -2.0, v244, v144
	v_fma_f32 v145, -2.0, v247, v145
	v_fma_f32 v146, -2.0, v250, v146
	v_fma_f32 v147, -2.0, v253, v147
	v_mul_f32_e32 v132, v132, v140
	v_mul_f32_e32 v133, v133, v141
	v_mul_f32_e32 v134, v134, v142
	v_mul_f32_e32 v135, v135, v143
	v_rcp_f32_e32 v132, v132
	v_rcp_f32_e32 v133, v133
	v_rcp_f32_e32 v134, v134
	v_rcp_f32_e32 v135, v135
	v_mul_f32_e32 v136, v136, v144
	v_mul_f32_e32 v137, v137, v145
	v_mul_f32_e32 v138, v138, v146
	v_mul_f32_e32 v139, v139, v147
	v_fma_f32 v19, v136, v132, v19
	v_fma_f32 v20, v137, v133, v20
	v_fma_f32 v21, v138, v134, v21
	v_fma_f32 v22, v139, v135, v22
	v_mul_f32_e32 v244, v148, v152
	v_mul_f32_e32 v247, v149, v153
	v_mul_f32_e32 v250, v150, v154
	v_mul_f32_e32 v253, v151, v155
	v_mul_f32_e64 v245, -v152, v152
	v_mul_f32_e64 v248, -v153, v153
	v_mul_f32_e64 v251, -v154, v154
	v_mul_f32_e64 v254, -v155, v155
	v_add_f32_e32 v246, v148, v152
	v_add_f32_e32 v249, v149, v153
	v_add_f32_e32 v252, v150, v154
	v_add_f32_e32 v255, v151, v155
	v_fma_f32 v245, -v148, v148, v245
	v_fma_f32 v248, -v149, v149, v248
	v_fma_f32 v251, -v150, v150, v251
	v_fma_f32 v254, -v151, v151, v254
	v_fma_f32 v148, v10, v246, v11
	v_fma_f32 v149, v10, v249, v11
	v_fma_f32 v150, v10, v252, v11
	v_fma_f32 v151, v10, v255, v11
	v_fma_f32 v160, v13, v160, v14
	v_fma_f32 v161, v13, v161, v14
	v_fma_f32 v162, v13, v162, v14
	v_fma_f32 v163, v13, v163, v14
	v_fma_f32 v156, v12, v156, v245
	v_fma_f32 v157, v12, v157, v248
	v_fma_f32 v158, v12, v158, v251
	v_fma_f32 v159, v12, v159, v254
	v_fma_f32 v152, 2.0, v244, v148
	v_fma_f32 v153, 2.0, v247, v149
	v_fma_f32 v154, 2.0, v250, v150
	v_fma_f32 v155, 2.0, v253, v151
	v_sub_f32_e32 v148, v148, v245
	v_sub_f32_e32 v149, v149, v248
	v_sub_f32_e32 v150, v150, v251
	v_sub_f32_e32 v151, v151, v254
	v_fma_f32 v160, -2.0, v244, v160
	v_fma_f32 v161, -2.0, v247, v161
	v_fma_f32 v162, -2.0, v250, v162
	v_fma_f32 v163, -2.0, v253, v163
	v_mul_f32_e32 v148, v148, v156
	v_mul_f32_e32 v149, v149, v157
	v_mul_f32_e32 v150, v150, v158
	v_mul_f32_e32 v151, v151, v159
	v_rcp_f32_e32 v148, v148
	v_rcp_f32_e32 v149, v149
	v_rcp_f32_e32 v150, v150
	v_rcp_f32_e32 v151, v151
	v_mul_f32_e32 v152, v152, v160
	v_mul_f32_e32 v153, v153, v161
	v_mul_f32_e32 v154, v154, v162
	v_mul_f32_e32 v155, v155, v163
	v_mul_f32_e32 v152, v152, v148
	v_mul_f32_e32 v153, v153, v149
	v_mul_f32_e32 v154, v154, v150
	v_mul_f32_e32 v155, v155, v151
	v_fma_f32 v19, v152, v15, v19
	v_fma_f32 v20, v153, v16, v20
	v_fma_f32 v21, v154, v17, v21
	v_fma_f32 v22, v155, v18, v22
	v_add_f32_e32 v19, v19, v20
	v_add_f32_e32 v21, v21, v22
	v_add_f32_e32 v23, v19, v21
	v_mov_b32_e32 v19, 0
	v_mov_b32_e32 v20, 0
	v_mov_b32_e32 v21, 0
	v_mov_b32_e32 v22, 0
	s_waitcnt vmcnt(4)
	v_cvt_pk_f16_f32 v100, v164, v168
	v_cvt_pk_f16_f32 v116, v180, v184
	v_pk_add_f16 v100, v100, -0.5 op_sel_hi:[1,0]
	v_pk_add_f16 v116, v116, -0.5 op_sel_hi:[1,0]
	v_pk_mul_f16 v132, v116, v116
	v_pk_mul_f16 v148, v100, v116
	v_pk_fma_f16 v132, v100, v100, v132
	v_cvt_pk_f16_f32 v104, v165, v169
	v_cvt_pk_f16_f32 v120, v181, v185
	v_pk_add_f16 v104, v104, -0.5 op_sel_hi:[1,0]
	v_pk_add_f16 v120, v120, -0.5 op_sel_hi:[1,0]
	v_pk_mul_f16 v136, v120, v120
	v_pk_mul_f16 v152, v104, v120
	v_pk_fma_f16 v136, v104, v104, v136
	v_cvt_pk_f16_f32 v108, v166, v170
	v_cvt_pk_f16_f32 v124, v182, v186
	v_pk_add_f16 v108, v108, -0.5 op_sel_hi:[1,0]
	v_pk_add_f16 v124, v124, -0.5 op_sel_hi:[1,0]
	v_pk_mul_f16 v140, v124, v124
	v_pk_mul_f16 v156, v108, v124
	v_pk_fma_f16 v140, v108, v108, v140
	v_cvt_pk_f16_f32 v112, v167, v171
	v_cvt_pk_f16_f32 v128, v183, v187
	v_pk_add_f16 v112, v112, -0.5 op_sel_hi:[1,0]
	v_pk_add_f16 v128, v128, -0.5 op_sel_hi:[1,0]
	v_pk_mul_f16 v144, v128, v128
	v_pk_mul_f16 v160, v112, v128
	v_pk_fma_f16 v144, v112, v112, v144
	s_waitcnt vmcnt(0)
	v_cvt_pk_f16_f32 v101, v172, v176
	v_cvt_pk_f16_f32 v117, v188, v192
	v_pk_add_f16 v101, v101, -0.5 op_sel_hi:[1,0]
	v_pk_add_f16 v117, v117, -0.5 op_sel_hi:[1,0]
	v_pk_mul_f16 v133, v117, v117
	v_pk_mul_f16 v149, v101, v117
	v_pk_fma_f16 v133, v101, v101, v133
	v_cvt_pk_f16_f32 v105, v173, v177
	v_cvt_pk_f16_f32 v121, v189, v193
	v_pk_add_f16 v105, v105, -0.5 op_sel_hi:[1,0]
	v_pk_add_f16 v121, v121, -0.5 op_sel_hi:[1,0]
	v_pk_mul_f16 v137, v121, v121
	v_pk_mul_f16 v153, v105, v121
	v_pk_fma_f16 v137, v105, v105, v137
	v_cvt_pk_f16_f32 v109, v174, v178
	v_cvt_pk_f16_f32 v125, v190, v194
	v_pk_add_f16 v109, v109, -0.5 op_sel_hi:[1,0]
	v_pk_add_f16 v125, v125, -0.5 op_sel_hi:[1,0]
	v_pk_mul_f16 v141, v125, v125
	v_pk_mul_f16 v157, v109, v125
	v_pk_fma_f16 v141, v109, v109, v141
	v_cvt_pk_f16_f32 v113, v175, v179
	v_cvt_pk_f16_f32 v129, v191, v195
	v_pk_add_f16 v113, v113, -0.5 op_sel_hi:[1,0]
	v_pk_add_f16 v129, v129, -0.5 op_sel_hi:[1,0]
	v_pk_mul_f16 v145, v129, v129
	v_pk_mul_f16 v161, v113, v129
	v_pk_fma_f16 v145, v113, v113, v145
	v_xor_b32_e32 v9, 32, v8
	v_lshlrev_b32_e32 v9, 2, v9
	ds_bpermute_b32 v102, v9, v100
	ds_bpermute_b32 v103, v9, v101
	ds_bpermute_b32 v106, v9, v104
	ds_bpermute_b32 v107, v9, v105
	ds_bpermute_b32 v110, v9, v108
	ds_bpermute_b32 v111, v9, v109
	ds_bpermute_b32 v114, v9, v112
	ds_bpermute_b32 v115, v9, v113
	s_waitcnt lgkmcnt(0)
	ds_bpermute_b32 v118, v9, v116
	ds_bpermute_b32 v119, v9, v117
	ds_bpermute_b32 v122, v9, v120
	ds_bpermute_b32 v123, v9, v121
	ds_bpermute_b32 v126, v9, v124
	ds_bpermute_b32 v127, v9, v125
	ds_bpermute_b32 v130, v9, v128
	ds_bpermute_b32 v131, v9, v129
	s_waitcnt lgkmcnt(0)
	ds_bpermute_b32 v134, v9, v132
	ds_bpermute_b32 v135, v9, v133
	ds_bpermute_b32 v138, v9, v136
	ds_bpermute_b32 v139, v9, v137
	ds_bpermute_b32 v142, v9, v140
	ds_bpermute_b32 v143, v9, v141
	ds_bpermute_b32 v146, v9, v144
	ds_bpermute_b32 v147, v9, v145
	s_waitcnt lgkmcnt(0)
	ds_bpermute_b32 v150, v9, v148
	ds_bpermute_b32 v151, v9, v149
	ds_bpermute_b32 v154, v9, v152
	ds_bpermute_b32 v155, v9, v153
	ds_bpermute_b32 v158, v9, v156
	ds_bpermute_b32 v159, v9, v157
	ds_bpermute_b32 v162, v9, v160
	ds_bpermute_b32 v163, v9, v161
	s_waitcnt lgkmcnt(0)
	v_mfma_f32_16x16x32_f16 v[196:199], v[36:39], v[28:31], 0
	v_mfma_f32_16x16x32_f16 v[200:203], v[40:43], v[28:31], 0
	v_mfma_f32_16x16x32_f16 v[204:207], v[44:47], v[28:31], 0
	v_mfma_f32_16x16x32_f16 v[208:211], v[48:51], v[28:31], 0
	v_mfma_f32_16x16x32_f16 v[196:199], v[100:103], v[32:35], v[196:199]
	v_mfma_f32_16x16x32_f16 v[200:203], v[104:107], v[32:35], v[200:203]
	v_mfma_f32_16x16x32_f16 v[204:207], v[108:111], v[32:35], v[204:207]
	v_mfma_f32_16x16x32_f16 v[208:211], v[112:115], v[32:35], v[208:211]
	v_mfma_f32_16x16x32_f16 v[212:215], v[52:55], v[28:31], 0
	v_mfma_f32_16x16x32_f16 v[216:219], v[56:59], v[28:31], 0
	v_mfma_f32_16x16x32_f16 v[220:223], v[60:63], v[28:31], 0
	v_mfma_f32_16x16x32_f16 v[224:227], v[64:67], v[28:31], 0
	v_mfma_f32_16x16x32_f16 v[212:215], v[116:119], v[32:35], v[212:215]
	v_mfma_f32_16x16x32_f16 v[216:219], v[120:123], v[32:35], v[216:219]
	v_mfma_f32_16x16x32_f16 v[220:223], v[124:127], v[32:35], v[220:223]
	v_mfma_f32_16x16x32_f16 v[224:227], v[128:131], v[32:35], v[224:227]
	v_cvt_pk_f16_f32 v164, v196, v200
	v_cvt_pk_f16_f32 v165, v204, v208
	v_cvt_pk_f16_f32 v166, v197, v201
	v_cvt_pk_f16_f32 v167, v205, v209
	v_cvt_pk_f16_f32 v168, v198, v202
	v_cvt_pk_f16_f32 v169, v206, v210
	v_cvt_pk_f16_f32 v170, v199, v203
	v_cvt_pk_f16_f32 v171, v207, v211
	v_mfma_f32_16x16x32_f16 v[196:199], v[68:71], v[28:31], 0
	v_mfma_f32_16x16x32_f16 v[200:203], v[72:75], v[28:31], 0
	v_mfma_f32_16x16x32_f16 v[204:207], v[76:79], v[28:31], 0
	v_mfma_f32_16x16x32_f16 v[208:211], v[80:83], v[28:31], 0
	v_mfma_f32_16x16x32_f16 v[196:199], v[132:135], v[32:35], v[196:199]
	v_mfma_f32_16x16x32_f16 v[200:203], v[136:139], v[32:35], v[200:203]
	v_mfma_f32_16x16x32_f16 v[204:207], v[140:143], v[32:35], v[204:207]
	v_mfma_f32_16x16x32_f16 v[208:211], v[144:147], v[32:35], v[208:211]
	v_cvt_pk_f16_f32 v172, v212, v216
	v_cvt_pk_f16_f32 v173, v220, v224
	v_cvt_pk_f16_f32 v174, v213, v217
	v_cvt_pk_f16_f32 v175, v221, v225
	v_cvt_pk_f16_f32 v176, v214, v218
	v_cvt_pk_f16_f32 v177, v222, v226
	v_cvt_pk_f16_f32 v178, v215, v219
	v_cvt_pk_f16_f32 v179, v223, v227
	v_mfma_f32_16x16x32_f16 v[212:215], v[84:87], v[28:31], 0
	v_mfma_f32_16x16x32_f16 v[216:219], v[88:91], v[28:31], 0
	v_mfma_f32_16x16x32_f16 v[220:223], v[92:95], v[28:31], 0
	v_mfma_f32_16x16x32_f16 v[224:227], v[96:99], v[28:31], 0
	v_mfma_f32_16x16x32_f16 v[212:215], v[148:151], v[32:35], v[212:215]
	v_mfma_f32_16x16x32_f16 v[216:219], v[152:155], v[32:35], v[216:219]
	v_mfma_f32_16x16x32_f16 v[220:223], v[156:159], v[32:35], v[220:223]
	v_mfma_f32_16x16x32_f16 v[224:227], v[160:163], v[32:35], v[224:227]
	v_cvt_pk_f16_f32 v180, v196, v200
	v_cvt_pk_f16_f32 v181, v204, v208
	v_cvt_pk_f16_f32 v182, v197, v201
	v_cvt_pk_f16_f32 v183, v205, v209
	v_cvt_pk_f16_f32 v184, v198, v202
	v_cvt_pk_f16_f32 v185, v206, v210
	v_cvt_pk_f16_f32 v186, v199, v203
	v_cvt_pk_f16_f32 v187, v207, v211
	v_cvt_pk_f16_f32 v188, v212, v216
	v_cvt_pk_f16_f32 v189, v220, v224
	v_cvt_pk_f16_f32 v190, v213, v217
	v_cvt_pk_f16_f32 v191, v221, v225
	v_cvt_pk_f16_f32 v192, v214, v218
	v_cvt_pk_f16_f32 v193, v222, v226
	v_cvt_pk_f16_f32 v194, v215, v219
	v_cvt_pk_f16_f32 v195, v223, v227
	s_mov_b64 exec, s[38:39]
	ds_write_b128 v4, v[168:171] offset:49152
	ds_write_b128 v4, v[176:179] offset:49664
	ds_write_b128 v4, v[184:187] offset:50176
	ds_write_b128 v4, v[192:195] offset:50688
	s_mov_b64 exec, -1
	v_mfma_f32_16x16x32_f16 v[196:199], v[24:27], v[164:167], 0
	v_mfma_f32_16x16x32_f16 v[200:203], v[24:27], v[172:175], 0
	v_mfma_f32_16x16x32_f16 v[204:207], v[24:27], v[180:183], v[0:3]
	v_mfma_f32_16x16x32_f16 v[208:211], v[24:27], v[188:191], 0
	v_mfma_f32_16x16x32_f16 v[212:215], v[28:31], v[164:167], 0
	v_mfma_f32_16x16x32_f16 v[216:219], v[28:31], v[172:175], 0
	v_mfma_f32_16x16x32_f16 v[220:223], v[28:31], v[180:183], v[0:3]
	v_mfma_f32_16x16x32_f16 v[224:227], v[28:31], v[188:191], 0
	v_mfma_f32_16x16x32_f16 v[212:215], v[32:35], v[168:171], v[212:215]
	v_mfma_f32_16x16x32_f16 v[216:219], v[32:35], v[176:179], v[216:219]
	v_mfma_f32_16x16x32_f16 v[220:223], v[32:35], v[184:187], v[220:223]
	v_mfma_f32_16x16x32_f16 v[224:227], v[32:35], v[192:195], v[224:227]
	s_waitcnt lgkmcnt(0)
	ds_write_b32 v6, v6 offset:96
	ds_read_b32 v9, v7 offset:96
	v_mul_f32_e32 v244, v196, v200
	v_mul_f32_e32 v247, v197, v201
	v_mul_f32_e32 v250, v198, v202
	v_mul_f32_e32 v253, v199, v203
	v_mul_f32_e64 v245, -v200, v200
	v_mul_f32_e64 v248, -v201, v201
	v_mul_f32_e64 v251, -v202, v202
	v_mul_f32_e64 v254, -v203, v203
	v_add_f32_e32 v246, v196, v200
	v_add_f32_e32 v249, v197, v201
	v_add_f32_e32 v252, v198, v202
	v_add_f32_e32 v255, v199, v203
	v_fma_f32 v245, -v196, v196, v245
	v_fma_f32 v248, -v197, v197, v248
	v_fma_f32 v251, -v198, v198, v251
	v_fma_f32 v254, -v199, v199, v254
	v_fma_f32 v196, v10, v246, v11
	v_fma_f32 v197, v10, v249, v11
	v_fma_f32 v198, v10, v252, v11
	v_fma_f32 v199, v10, v255, v11
	v_fma_f32 v208, v13, v208, v14
	v_fma_f32 v209, v13, v209, v14
	v_fma_f32 v210, v13, v210, v14
	v_fma_f32 v211, v13, v211, v14
	v_fma_f32 v204, v12, v204, v245
	v_fma_f32 v205, v12, v205, v248
	v_fma_f32 v206, v12, v206, v251
	v_fma_f32 v207, v12, v207, v254
	v_fma_f32 v200, 2.0, v244, v196
	v_fma_f32 v201, 2.0, v247, v197
	v_fma_f32 v202, 2.0, v250, v198
	v_fma_f32 v203, 2.0, v253, v199
	v_sub_f32_e32 v196, v196, v245
	v_sub_f32_e32 v197, v197, v248
	v_sub_f32_e32 v198, v198, v251
	v_sub_f32_e32 v199, v199, v254
	v_fma_f32 v208, -2.0, v244, v208
	v_fma_f32 v209, -2.0, v247, v209
	v_fma_f32 v210, -2.0, v250, v210
	v_fma_f32 v211, -2.0, v253, v211
	v_mul_f32_e32 v196, v196, v204
	v_mul_f32_e32 v197, v197, v205
	v_mul_f32_e32 v198, v198, v206
	v_mul_f32_e32 v199, v199, v207
	v_rcp_f32_e32 v196, v196
	v_rcp_f32_e32 v197, v197
	v_rcp_f32_e32 v198, v198
	v_rcp_f32_e32 v199, v199
	v_mul_f32_e32 v200, v200, v208
	v_mul_f32_e32 v201, v201, v209
	v_mul_f32_e32 v202, v202, v210
	v_mul_f32_e32 v203, v203, v211
	v_fma_f32 v19, v200, v196, v19
	v_fma_f32 v20, v201, v197, v20
	v_fma_f32 v21, v202, v198, v21
	v_fma_f32 v22, v203, v199, v22
	v_mfma_f32_16x16x32_f16 v[196:199], v[24:27], v[168:171], 0
	v_mfma_f32_16x16x32_f16 v[200:203], v[24:27], v[176:179], 0
	v_mfma_f32_16x16x32_f16 v[204:207], v[24:27], v[184:187], v[0:3]
	v_mfma_f32_16x16x32_f16 v[208:211], v[24:27], v[192:195], 0
	s_waitcnt lgkmcnt(0)
	v_cmp_ne_u32_e32 vcc, 0, v9
	s_cbranch_vccnz .Lq_go_3

.Lq_go_3:
	ds_read_b128 v[228:231], v5 offset:49152
	ds_read_b128 v[232:235], v5 offset:49664
	ds_read_b128 v[236:239], v5 offset:50176
	ds_read_b128 v[240:243], v5 offset:50688
	v_mul_f32_e32 v244, v212, v216
	v_mul_f32_e32 v247, v213, v217
	v_mul_f32_e32 v250, v214, v218
	v_mul_f32_e32 v253, v215, v219
	v_mul_f32_e64 v245, -v216, v216
	v_mul_f32_e64 v248, -v217, v217
	v_mul_f32_e64 v251, -v218, v218
	v_mul_f32_e64 v254, -v219, v219
	v_add_f32_e32 v246, v212, v216
	v_add_f32_e32 v249, v213, v217
	v_add_f32_e32 v252, v214, v218
	v_add_f32_e32 v255, v215, v219
	v_fma_f32 v245, -v212, v212, v245
	v_fma_f32 v248, -v213, v213, v248
	v_fma_f32 v251, -v214, v214, v251
	v_fma_f32 v254, -v215, v215, v254
	v_fma_f32 v212, v10, v246, v11
	v_fma_f32 v213, v10, v249, v11
	v_fma_f32 v214, v10, v252, v11
	v_fma_f32 v215, v10, v255, v11
	v_fma_f32 v224, v13, v224, v14
	v_fma_f32 v225, v13, v225, v14
	v_fma_f32 v226, v13, v226, v14
	v_fma_f32 v227, v13, v227, v14
	v_fma_f32 v220, v12, v220, v245
	v_fma_f32 v221, v12, v221, v248
	v_fma_f32 v222, v12, v222, v251
	v_fma_f32 v223, v12, v223, v254
	v_fma_f32 v216, 2.0, v244, v212
	v_fma_f32 v217, 2.0, v247, v213
	v_fma_f32 v218, 2.0, v250, v214
	v_fma_f32 v219, 2.0, v253, v215
	v_sub_f32_e32 v212, v212, v245
	v_sub_f32_e32 v213, v213, v248
	v_sub_f32_e32 v214, v214, v251
	v_sub_f32_e32 v215, v215, v254
	v_fma_f32 v224, -2.0, v244, v224
	v_fma_f32 v225, -2.0, v247, v225
	v_fma_f32 v226, -2.0, v250, v226
	v_fma_f32 v227, -2.0, v253, v227
	v_mul_f32_e32 v212, v212, v220
	v_mul_f32_e32 v213, v213, v221
	v_mul_f32_e32 v214, v214, v222
	v_mul_f32_e32 v215, v215, v223
	v_rcp_f32_e32 v212, v212
	v_rcp_f32_e32 v213, v213
	v_rcp_f32_e32 v214, v214
	v_rcp_f32_e32 v215, v215
	v_mul_f32_e32 v216, v216, v224
	v_mul_f32_e32 v217, v217, v225
	v_mul_f32_e32 v218, v218, v226
	v_mul_f32_e32 v219, v219, v227
	v_fma_f32 v19, v216, v212, v19
	v_fma_f32 v20, v217, v213, v20
	v_fma_f32 v21, v218, v214, v21
	v_fma_f32 v22, v219, v215, v22
	s_waitcnt lgkmcnt(0)
	v_mfma_f32_16x16x32_f16 v[212:215], v[28:31], v[228:231], 0
	v_mfma_f32_16x16x32_f16 v[216:219], v[28:31], v[232:235], 0
	v_mfma_f32_16x16x32_f16 v[220:223], v[28:31], v[236:239], v[0:3]
	v_mfma_f32_16x16x32_f16 v[224:227], v[28:31], v[240:243], 0
	v_mfma_f32_16x16x32_f16 v[212:215], v[32:35], v[164:167], v[212:215]
	v_mfma_f32_16x16x32_f16 v[216:219], v[32:35], v[172:175], v[216:219]
	v_mfma_f32_16x16x32_f16 v[220:223], v[32:35], v[180:183], v[220:223]
	v_mfma_f32_16x16x32_f16 v[224:227], v[32:35], v[188:191], v[224:227]
	v_mul_f32_e32 v244, v196, v200
	v_mul_f32_e32 v247, v197, v201
	v_mul_f32_e32 v250, v198, v202
	v_mul_f32_e32 v253, v199, v203
	v_mul_f32_e64 v245, -v200, v200
	v_mul_f32_e64 v248, -v201, v201
	v_mul_f32_e64 v251, -v202, v202
	v_mul_f32_e64 v254, -v203, v203
	v_add_f32_e32 v246, v196, v200
	v_add_f32_e32 v249, v197, v201
	v_add_f32_e32 v252, v198, v202
	v_add_f32_e32 v255, v199, v203
	v_fma_f32 v245, -v196, v196, v245
	v_fma_f32 v248, -v197, v197, v248
	v_fma_f32 v251, -v198, v198, v251
	v_fma_f32 v254, -v199, v199, v254
	v_fma_f32 v196, v10, v246, v11
	v_fma_f32 v197, v10, v249, v11
	v_fma_f32 v198, v10, v252, v11
	v_fma_f32 v199, v10, v255, v11
	v_fma_f32 v208, v13, v208, v14
	v_fma_f32 v209, v13, v209, v14
	v_fma_f32 v210, v13, v210, v14
	v_fma_f32 v211, v13, v211, v14
	v_fma_f32 v204, v12, v204, v245
	v_fma_f32 v205, v12, v205, v248
	v_fma_f32 v206, v12, v206, v251
	v_fma_f32 v207, v12, v207, v254
	v_fma_f32 v200, 2.0, v244, v196
	v_fma_f32 v201, 2.0, v247, v197
	v_fma_f32 v202, 2.0, v250, v198
	v_fma_f32 v203, 2.0, v253, v199
	v_sub_f32_e32 v196, v196, v245
	v_sub_f32_e32 v197, v197, v248
	v_sub_f32_e32 v198, v198, v251
	v_sub_f32_e32 v199, v199, v254
	v_fma_f32 v208, -2.0, v244, v208
	v_fma_f32 v209, -2.0, v247, v209
	v_fma_f32 v210, -2.0, v250, v210
	v_fma_f32 v211, -2.0, v253, v211
	v_mul_f32_e32 v196, v196, v204
	v_mul_f32_e32 v197, v197, v205
	v_mul_f32_e32 v198, v198, v206
	v_mul_f32_e32 v199, v199, v207
	v_rcp_f32_e32 v196, v196
	v_rcp_f32_e32 v197, v197
	v_rcp_f32_e32 v198, v198
	v_rcp_f32_e32 v199, v199
	v_mul_f32_e32 v200, v200, v208
	v_mul_f32_e32 v201, v201, v209
	v_mul_f32_e32 v202, v202, v210
	v_mul_f32_e32 v203, v203, v211
	v_fma_f32 v19, v200, v196, v19
	v_fma_f32 v20, v201, v197, v20
	v_fma_f32 v21, v202, v198, v21
	v_fma_f32 v22, v203, v199, v22
	v_mul_f32_e32 v244, v212, v216
	v_mul_f32_e32 v247, v213, v217
	v_mul_f32_e32 v250, v214, v218
	v_mul_f32_e32 v253, v215, v219
	v_mul_f32_e64 v245, -v216, v216
	v_mul_f32_e64 v248, -v217, v217
	v_mul_f32_e64 v251, -v218, v218
	v_mul_f32_e64 v254, -v219, v219
	v_add_f32_e32 v246, v212, v216
	v_add_f32_e32 v249, v213, v217
	v_add_f32_e32 v252, v214, v218
	v_add_f32_e32 v255, v215, v219
	v_fma_f32 v245, -v212, v212, v245
	v_fma_f32 v248, -v213, v213, v248
	v_fma_f32 v251, -v214, v214, v251
	v_fma_f32 v254, -v215, v215, v254
	v_fma_f32 v212, v10, v246, v11
	v_fma_f32 v213, v10, v249, v11
	v_fma_f32 v214, v10, v252, v11
	v_fma_f32 v215, v10, v255, v11
	v_fma_f32 v224, v13, v224, v14
	v_fma_f32 v225, v13, v225, v14
	v_fma_f32 v226, v13, v226, v14
	v_fma_f32 v227, v13, v227, v14
	v_fma_f32 v220, v12, v220, v245
	v_fma_f32 v221, v12, v221, v248
	v_fma_f32 v222, v12, v222, v251
	v_fma_f32 v223, v12, v223, v254
	v_fma_f32 v216, 2.0, v244, v212
	v_fma_f32 v217, 2.0, v247, v213
	v_fma_f32 v218, 2.0, v250, v214
	v_fma_f32 v219, 2.0, v253, v215
	v_sub_f32_e32 v212, v212, v245
	v_sub_f32_e32 v213, v213, v248
	v_sub_f32_e32 v214, v214, v251
	v_sub_f32_e32 v215, v215, v254
	v_fma_f32 v224, -2.0, v244, v224
	v_fma_f32 v225, -2.0, v247, v225
	v_fma_f32 v226, -2.0, v250, v226
	v_fma_f32 v227, -2.0, v253, v227
	v_mul_f32_e32 v212, v212, v220
	v_mul_f32_e32 v213, v213, v221
	v_mul_f32_e32 v214, v214, v222
	v_mul_f32_e32 v215, v215, v223
	v_rcp_f32_e32 v212, v212
	v_rcp_f32_e32 v213, v213
	v_rcp_f32_e32 v214, v214
	v_rcp_f32_e32 v215, v215
	v_mul_f32_e32 v216, v216, v224
	v_mul_f32_e32 v217, v217, v225
	v_mul_f32_e32 v218, v218, v226
	v_mul_f32_e32 v219, v219, v227
	v_mul_f32_e32 v216, v216, v212
	v_mul_f32_e32 v217, v217, v213
	v_mul_f32_e32 v218, v218, v214
	v_mul_f32_e32 v219, v219, v215
	v_fma_f32 v19, v216, v15, v19
	v_fma_f32 v20, v217, v16, v20
	v_fma_f32 v21, v218, v17, v21
	v_fma_f32 v22, v219, v18, v22
	v_add_f32_e32 v19, v19, v20
	v_add_f32_e32 v21, v21, v22
	v_add_f32_e32 v21, v19, v21
	v_and_b32_e32 v9, 15, v8
	s_cmp_eq_u32 s15, 7
	s_cselect_b32 s23, 6, 16
	v_cmp_gt_u32_e32 vcc, s23, v9
	s_nop 1
	v_cndmask_b32_e32 v21, 0, v21, vcc
	v_add_f32_e32 v19, v23, v21
	s_nop 1
	v_add_f32_dpp v19, v19, v19 quad_perm:[1,0,3,2] row_mask:0xf bank_mask:0xf
	s_nop 1
	v_add_f32_dpp v19, v19, v19 quad_perm:[2,3,0,1] row_mask:0xf bank_mask:0xf
	s_nop 1
	v_add_f32_dpp v19, v19, v19 row_half_mirror row_mask:0xf bank_mask:0xf
	s_nop 1
	v_add_f32_dpp v19, v19, v19 row_mirror row_mask:0xf bank_mask:0xf
	s_nop 0
	v_readlane_b32 s40, v19, 0
	v_readlane_b32 s41, v19, 16
	v_readlane_b32 s42, v19, 32
	v_readlane_b32 s43, v19, 48
	s_lshl_b32 s24, s2, 3
	s_add_u32 s24, s24, s12
	s_lshl_b32 s24, s24, 2
	v_mov_b32_e32 v19, s40
	v_add_f32_e32 v19, s41, v19
	v_add_f32_e32 v19, s42, v19
	v_add_f32_e32 v19, s43, v19
	v_mov_b32_e32 v9, s24
	v_cmp_eq_u32_e32 vcc, 0, v8
	s_nop 1
	s_and_saveexec_b64 s[30:31], vcc
	global_store_dword v9, v19, s[10:11] sc0 sc1
	s_endpgm
